# attention main loop: -mhat enters through the MFMA C operand (16-reg block, live-through regs parked in LDS), 64 v_sub per iteration dropped
# speedup vs baseline: 1.0147x; 1.0085x over previous
.LBB0_1026:
	s_or_b64 exec, exec, s[4:5]
	v_mov_b32_e32 v2, s2
	s_waitcnt lgkmcnt(0)
	s_barrier
	ds_read_b32 v2, v2
	s_mov_b64 s[4:5], -1
	s_waitcnt lgkmcnt(0)
	s_barrier
	v_readfirstlane_b32 s7, v2
	s_cmpk_gt_i32 s7, 0x7f
	s_cbranch_scc1 .LBB0_1021
	s_ashr_i32 s6, s7, 5
	s_add_i32 s8, s6, s28
	s_ashr_i32 s4, s8, 3
	s_ashr_i32 s5, s4, 31
	s_lshl_b64 s[90:91], s[4:5], 12
	s_lshl_b32 s5, s7, 7
	s_and_b32 s5, s5, 0xf80
	s_or_b32 s90, s90, s5
	s_mul_i32 s5, s91, 0x3400
	s_mul_hi_u32 s7, s90, 0x3400
	s_add_i32 s7, s7, s5
	s_mul_i32 s5, s90, 0x3400
	s_add_u32 s5, s13, s5
	s_addc_u32 s7, s94, s7
	s_lshl_b32 s8, s8, 7
	s_and_b32 s29, s8, 0x380
	s_lshl_b32 s10, s29, 1
	s_add_u32 s8, s5, s10
	s_addc_u32 s9, s7, 0
	s_mul_i32 s11, s4, 0x3400000
	s_mul_hi_i32 s7, s4, 0x3400000
	s_add_u32 s4, s13, s11
	s_addc_u32 s5, s94, s7
	s_add_u32 s4, s4, s10
	v_readfirstlane_b32 s10, v238
	s_addc_u32 s5, s5, 0
	s_ashr_i32 s20, s10, 6
	v_lshl_or_b32 v6, s20, 3, v241
	v_mov_b64_e32 v[2:3], s[4:5]
	v_mad_i64_i32 v[4:5], s[44:45], v6, s83, v[2:3]
	v_lshl_add_u64 v[50:51], v[4:5], 0, v[0:1]
	v_or_b32_e32 v4, 4, v6
	s_and_b32 s24, s20, 1
	v_mad_i64_i32 v[2:3], s[44:45], v4, s83, v[2:3]
	v_mov_b32_e32 v205, v1
	s_ashr_i32 s25, s10, 7
	v_lshl_add_u64 v[54:55], v[2:3], 0, v[204:205]
	v_lshl_or_b32 v2, s24, 5, v242
	s_mov_b32 s72, s88
	v_mul_u32_u24_e32 v2, 0x1a00, v2
	s_lshl_b32 s88, s25, 5
	v_lshlrev_b32_e32 v52, 1, v2
	v_mov_b32_e32 v53, v1
	s_ashr_i32 s89, s88, 31
	s_and_b32 s71, s10, 0x3fffffc0
	v_lshl_add_u64 v[2:3], s[4:5], 0, v[52:53]
	s_lshl_b64 s[4:5], s[88:89], 1
	s_lshl_b32 s89, s20, 11
	s_cmp_lg_u32 0, -1
	s_cselect_b32 s10, 0, 0
	s_lshl_b32 s25, s25, 12
	v_lshl_add_u64 v[2:3], v[2:3], 0, s[4:5]
	v_mov_b32_e32 v207, v1
	s_add_i32 s89, s89, s10
	s_add_i32 s10, s10, s25
	s_lshl_b32 s20, s24, 11
	s_load_dwordx2 s[92:93], s[60:61], 0xc0
	v_lshl_add_u64 v[214:215], v[50:51], 0, s[30:31]
	v_lshl_add_u64 v[56:57], v[2:3], 0, v[206:207]
	s_add_i32 s70, s10, s20
	s_mov_b32 s10, m0
	s_mov_b32 m0, s89
	s_nop 0
	global_load_lds_dwordx4 v[214:215], off
	s_mov_b32 m0, s10
	s_add_i32 vcc_lo, s89, 0x400
	v_lshl_add_u64 v[216:217], v[54:55], 0, s[30:31]
	v_lshl_add_u64 v[2:3], v[56:57], 0, s[14:15]
	s_mov_b32 s10, m0
	s_mov_b32 m0, vcc_lo
	s_nop 0
	global_load_lds_dwordx4 v[216:217], off
	s_mov_b32 m0, s10
	s_mov_b64 s[44:45], 0x35000
	s_add_i32 s70, s70, 0xc000
	s_mov_b32 s10, m0
	s_mov_b32 m0, s70
	s_nop 0
	global_load_lds_dwordx4 v[2:3], off
	s_mov_b32 m0, s10
	v_lshl_add_u64 v[2:3], v[56:57], 0, s[44:45]
	s_add_i32 s10, s70, 0x400
	s_mov_b32 s44, m0
	s_mov_b32 m0, s10
	s_nop 0
	global_load_lds_dwordx4 v[2:3], off
	s_mov_b32 m0, s44
	v_lshl_add_u64 v[2:3], v[50:51], 0, s[34:35]
	s_add_i32 s10, s89, 0x4000
	s_mov_b32 s44, m0
	s_mov_b32 m0, s10
	s_nop 0
	global_load_lds_dwordx4 v[2:3], off
	s_mov_b32 m0, s44
	v_lshl_add_u64 v[2:3], v[54:55], 0, s[34:35]
	s_add_i32 s10, s89, 0x4400
	s_mov_b32 s44, m0
	s_mov_b32 m0, s10
	s_nop 0
	global_load_lds_dwordx4 v[2:3], off
	s_mov_b32 m0, s44
	v_or_b32_e32 v4, s88, v240
	v_mov_b64_e32 v[2:3], s[8:9]
	s_lshl_b32 s20, s24, 7
	v_mad_i64_i32 v[2:3], s[8:9], v4, s83, v[2:3]
	v_lshl_add_u64 v[2:3], v[2:3], 0, s[20:21]
	v_mov_b32_e32 v209, v1
	v_lshl_add_u64 v[2:3], v[2:3], 0, v[208:209]
	global_load_dwordx4 v[158:161], v[2:3], off nt
	global_load_dwordx4 v[154:157], v[2:3], off offset:32 nt
	global_load_dwordx4 v[146:149], v[2:3], off offset:64 nt
	global_load_dwordx4 v[142:145], v[2:3], off offset:96 nt
	v_lshl_add_u64 v[2:3], v[50:51], 0, s[36:37]
	v_or_b32_e32 v6, s20, v245
	s_add_i32 s8, s89, 0x8000
	s_mov_b32 s10, m0
	s_mov_b32 m0, s8
	s_nop 0
	global_load_lds_dwordx4 v[2:3], off
	s_mov_b32 m0, s10
	v_lshl_add_u64 v[4:5], v[54:55], 0, s[36:37]
	v_bitop3_b32 v209, v6, v247, v246 bitop3:0xde
	s_add_i32 s9, s89, 0x8400
	s_mov_b32 s8, m0
	s_mov_b32 m0, s9
	s_nop 0
	global_load_lds_dwordx4 v[4:5], off
	s_mov_b32 m0, s8
	v_add_u32_e32 v211, 0, v209
	s_waitcnt vmcnt(6) lgkmcnt(0)
	s_barrier
	ds_read_b128 v[2:5], v211
	ds_read_b128 v[6:9], v211 offset:8192
	v_bitop3_b32 v10, s20, v246, v245 bitop3:0x36
	v_bitop3_b32 v213, v10, 32, v247 bitop3:0x36
	v_add_u32_e32 v250, 0, v213
	v_bitop3_b32 v251, v10, 64, v247 bitop3:0x36
	v_add_u32_e32 v252, 0, v251
	s_movk_i32 s20, 0x60
	v_bitop3_b32 v235, v10, s20, v247 bitop3:0x36
	v_add_u32_e32 v227, 0, v235
	s_mov_b32 s44, 0
	s_mov_b32 s45, s44
	s_mov_b32 s46, s44
	s_mov_b32 s47, s44
	s_mov_b32 s48, s44
	s_mov_b32 s49, s44
	s_mov_b32 s50, s44
	s_mov_b32 s51, s44
	s_mov_b32 s52, s44
	s_waitcnt vmcnt(3) lgkmcnt(0)
	v_mfma_f32_32x32x16_bf16 v[18:33], v[2:5], v[158:161], 0
	s_mov_b32 s53, s44
	s_mov_b32 s54, s44
	s_mov_b32 s55, s44
	s_mov_b32 s56, s44
	s_mov_b32 s57, s44
	s_mov_b32 s58, s44
	s_mov_b32 s59, s44
	v_mfma_f32_32x32x16_bf16 v[34:49], v[6:9], v[158:161], 0
	ds_read_b128 v[2:5], v250
	ds_read_b128 v[6:9], v250 offset:8192
	ds_read_b128 v[58:61], v227 offset:8192
	s_lshl_b32 s6, s6, 7
	s_add_i32 s6, s12, s6
	s_lshl_b32 s6, s6, 1
	s_and_b32 s6, s6, 0x700
	s_or_b32 s6, s11, s6
	s_waitcnt vmcnt(2) lgkmcnt(2)
	v_mfma_f32_32x32x16_bf16 v[18:33], v[2:5], v[154:157], v[18:33]
	ds_read_b128 v[2:5], v252
	v_lshl_add_u64 v[218:219], v[54:55], 0, s[16:17]
	v_lshl_add_u64 v[220:221], v[50:51], 0, s[16:17]
	s_mov_b32 s8, -1
	s_movk_i32 s10, 0x4000
	s_mov_b32 s9, 0x8000
	v_mov_b32_e32 v234, 0
	s_waitcnt lgkmcnt(2)
	v_mfma_f32_32x32x16_bf16 v[34:49], v[6:9], v[154:157], v[34:49]
	ds_read_b128 v[6:9], v252 offset:8192
	s_waitcnt vmcnt(1) lgkmcnt(1)
	v_mfma_f32_32x32x16_bf16 v[18:33], v[2:5], v[146:149], v[18:33]
	ds_read_b128 v[2:5], v227
	s_waitcnt vmcnt(0) lgkmcnt(0)
	s_barrier
	s_waitcnt lgkmcnt(1)
	v_mfma_f32_32x32x16_bf16 v[34:49], v[6:9], v[146:149], v[34:49]
	s_waitcnt vmcnt(0) lgkmcnt(0)
	v_mfma_f32_32x32x16_bf16 v[18:33], v[2:5], v[142:145], v[18:33]
	v_mov_b64_e32 v[2:3], s[44:45]
	v_mov_b64_e32 v[4:5], s[46:47]
	v_mov_b64_e32 v[6:7], s[48:49]
	v_mov_b64_e32 v[8:9], s[50:51]
	v_mov_b64_e32 v[10:11], s[52:53]
	v_mov_b64_e32 v[12:13], s[54:55]
	v_mov_b64_e32 v[14:15], s[56:57]
	v_mfma_f32_32x32x16_bf16 v[34:49], v[58:61], v[142:145], v[34:49]
	s_nop 3
	v_max_f32_e32 v58, v19, v19
	v_max_f32_e32 v59, v18, v18
	v_max_f32_e32 v58, v59, v58
	v_mov_b64_e32 v[16:17], s[58:59]
	s_mov_b64 s[46:47], 0xd1000
	s_nop 2
	v_max3_f32 v59, v20, v21, v35
	v_max3_f32 v58, v58, v34, v36
	v_max3_f32 v58, v58, v37, v22
	v_max3_f32 v59, v59, v24, v25
	v_max3_f32 v58, v58, v23, v38
	v_max3_f32 v59, v59, v40, v41
	v_max3_f32 v58, v58, v39, v26
	v_max3_f32 v59, v59, v28, v29
	v_max3_f32 v58, v58, v27, v42
	v_max3_f32 v59, v59, v44, v45
	v_max3_f32 v58, v58, v43, v30
	v_max3_f32 v59, v59, v32, v33
	v_max3_f32 v58, v58, v31, v46
	v_max3_f32 v59, v59, v48, v49
	v_max3_f32 v58, v58, v47, v59
	v_mov_b32_e32 v59, v58
	s_nop 1
	v_permlane32_swap_b32_e32 v58, v59
	v_max_f32_e32 v59, v59, v59
	v_max_f32_e32 v58, v58, v58
	v_max_f32_e32 v207, v58, v59
	v_sub_f32_e32 v18, v18, v207
	v_exp_f32_e32 v82, v18
	v_sub_f32_e32 v18, v34, v207
	v_exp_f32_e32 v66, v18
	v_sub_f32_e32 v18, v19, v207
	v_exp_f32_e32 v83, v18
	v_sub_f32_e32 v18, v35, v207
	v_exp_f32_e32 v67, v18
	v_sub_f32_e32 v18, v20, v207
	v_exp_f32_e32 v84, v18
	v_sub_f32_e32 v18, v36, v207
	v_exp_f32_e32 v68, v18
	v_sub_f32_e32 v18, v21, v207
	v_exp_f32_e32 v85, v18
	v_sub_f32_e32 v18, v37, v207
	v_exp_f32_e32 v69, v18
	v_sub_f32_e32 v18, v22, v207
	v_exp_f32_e32 v86, v18
	v_sub_f32_e32 v18, v38, v207
	v_exp_f32_e32 v70, v18
	v_sub_f32_e32 v18, v23, v207
	v_exp_f32_e32 v87, v18
	v_sub_f32_e32 v18, v39, v207
	v_exp_f32_e32 v71, v18
	v_sub_f32_e32 v18, v24, v207
	v_exp_f32_e32 v88, v18
	v_sub_f32_e32 v18, v40, v207
	v_exp_f32_e32 v72, v18
	v_sub_f32_e32 v18, v25, v207
	v_exp_f32_e32 v89, v18
	v_sub_f32_e32 v18, v41, v207
	v_exp_f32_e32 v73, v18
	v_sub_f32_e32 v18, v26, v207
	v_exp_f32_e32 v90, v18
	v_sub_f32_e32 v18, v42, v207
	v_exp_f32_e32 v74, v18
	v_sub_f32_e32 v18, v27, v207
	v_exp_f32_e32 v91, v18
	v_sub_f32_e32 v18, v43, v207
	v_exp_f32_e32 v75, v18
	v_sub_f32_e32 v18, v28, v207
	v_exp_f32_e32 v92, v18
	v_sub_f32_e32 v18, v44, v207
	v_exp_f32_e32 v76, v18
	v_sub_f32_e32 v18, v29, v207
	v_exp_f32_e32 v93, v18
	v_sub_f32_e32 v18, v45, v207
	v_exp_f32_e32 v77, v18
	v_sub_f32_e32 v18, v30, v207
	v_exp_f32_e32 v94, v18
	v_sub_f32_e32 v18, v46, v207
	v_exp_f32_e32 v78, v18
	v_sub_f32_e32 v18, v31, v207
	v_exp_f32_e32 v95, v18
	v_sub_f32_e32 v18, v47, v207
	v_exp_f32_e32 v79, v18
	v_sub_f32_e32 v18, v32, v207
	v_exp_f32_e32 v96, v18
	v_sub_f32_e32 v18, v48, v207
	v_exp_f32_e32 v80, v18
	v_sub_f32_e32 v18, v33, v207
	v_exp_f32_e32 v97, v18
	v_sub_f32_e32 v18, v49, v207
	v_exp_f32_e32 v81, v18
	v_lshl_add_u64 v[18:19], v[50:51], 0, s[18:19]
	s_mov_b32 s20, m0
	s_mov_b32 m0, s89
	s_nop 0
	global_load_lds_dwordx4 v[18:19], off
	s_mov_b32 m0, s20
	v_lshl_add_u64 v[18:19], v[54:55], 0, s[18:19]
	s_mov_b32 s20, m0
	s_mov_b32 m0, vcc_lo
	s_nop 0
	global_load_lds_dwordx4 v[18:19], off
	s_mov_b32 m0, s20
	v_lshl_add_u64 v[18:19], v[56:57], 0, s[46:47]
	s_add_i32 s20, s70, 0x4000
	s_mov_b32 s45, m0
	s_mov_b32 m0, s20
	s_nop 0
	global_load_lds_dwordx4 v[18:19], off
	s_mov_b32 m0, s45
	s_mov_b64 s[46:47], 0x105000
	v_lshl_add_u64 v[18:19], v[56:57], 0, s[46:47]
	s_add_i32 s20, s70, 0x4400
	s_mov_b32 s45, m0
	s_mov_b32 m0, s20
	s_nop 0
	global_load_lds_dwordx4 v[18:19], off
	s_mov_b32 m0, s45
	ds_read_b128 v[102:105], v211 offset:16384
	ds_read_b128 v[98:101], v211 offset:24576
	ds_read_b128 v[182:185], v250 offset:16384
	ds_read_b128 v[178:181], v250 offset:24576
	ds_read_b128 v[174:177], v252 offset:16384
	ds_read_b128 v[170:173], v252 offset:24576
	ds_read_b128 v[166:169], v227 offset:16384
	ds_read_b128 v[162:165], v227 offset:24576
	s_lshl_b32 s20, s71, 2
	s_add_i32 s20, s20, 0
	s_add_i32 s20, s20, 0x18000
	s_add_u32 s4, s6, s4
	s_waitcnt vmcnt(4) lgkmcnt(0)
	s_barrier
	s_addc_u32 s5, s7, s5
	v_lshl_add_u64 v[222:223], s[4:5], 0, v[52:53]
	v_mov_b64_e32 v[64:65], v[16:17]
	v_mov_b64_e32 v[48:49], v[16:17]
	v_mov_b64_e32 v[32:33], v[16:17]
	v_lshl_add_u32 v205, v240, 2, s20
	v_lshl_add_u64 v[224:225], v[200:201], 0, v[222:223]
	v_mov_b64_e32 v[62:63], v[14:15]
	v_mov_b64_e32 v[60:61], v[12:13]
	v_mov_b64_e32 v[58:59], v[10:11]
	v_mov_b64_e32 v[56:57], v[8:9]
	v_mov_b64_e32 v[54:55], v[6:7]
	v_mov_b64_e32 v[52:53], v[4:5]
	v_mov_b64_e32 v[50:51], v[2:3]
	v_mov_b64_e32 v[46:47], v[14:15]
	v_mov_b64_e32 v[44:45], v[12:13]
	v_mov_b64_e32 v[42:43], v[10:11]
	v_mov_b64_e32 v[40:41], v[8:9]
	v_mov_b64_e32 v[38:39], v[6:7]
	v_mov_b64_e32 v[36:37], v[4:5]
	v_mov_b64_e32 v[34:35], v[2:3]
	v_mov_b64_e32 v[30:31], v[14:15]
	v_mov_b64_e32 v[28:29], v[12:13]
	v_mov_b64_e32 v[26:27], v[10:11]
	v_mov_b64_e32 v[24:25], v[8:9]
	v_mov_b64_e32 v[22:23], v[6:7]
	v_mov_b64_e32 v[20:21], v[4:5]
	v_mov_b64_e32 v[18:19], v[2:3]
	v_mbcnt_lo_u32_b32 v230, -1, 0
	v_mbcnt_hi_u32_b32 v230, -1, v230
	v_and_b32_e32 v230, 32, v230
	v_lshl_add_u32 v230, v230, 2, v205
	ds_write_b32 v230, v237 offset:2048
	ds_write_b32 v230, v238 offset:4096
	ds_write_b32 v230, v239 offset:6144
	ds_write_b32 v230, v240 offset:8192
	ds_write_b32 v230, v241 offset:10240
	ds_write_b32 v230, v242 offset:12288
	ds_write_b32 v230, v244 offset:14336
	ds_write_b32 v230, v246 offset:16384
	s_waitcnt lgkmcnt(0)
	ds_write_b32 v230, v247 offset:18432
	ds_write_b32 v230, v248 offset:20480
	ds_write_b32 v230, v249 offset:22528
	ds_write_b32 v230, v250 offset:24576
	ds_write_b32 v230, v228 offset:26624
	ds_write_b32 v230, v229 offset:28672
	ds_write_b32 v230, v231 offset:30720
	s_waitcnt lgkmcnt(0)
	v_mov_b32_e32 v228, v243
	v_mov_b32_e32 v229, v245
	v_mov_b32_e32 v231, v251
	v_sub_f32_e32 v236, 0, v207
	v_sub_f32_e32 v237, 0, v207
	v_sub_f32_e32 v238, 0, v207
	v_sub_f32_e32 v239, 0, v207
	v_sub_f32_e32 v240, 0, v207
	v_sub_f32_e32 v241, 0, v207
	v_sub_f32_e32 v242, 0, v207
	v_sub_f32_e32 v243, 0, v207
	v_sub_f32_e32 v244, 0, v207
	v_sub_f32_e32 v245, 0, v207
	v_sub_f32_e32 v246, 0, v207
	v_sub_f32_e32 v247, 0, v207
	v_sub_f32_e32 v248, 0, v207
	v_sub_f32_e32 v249, 0, v207
	v_sub_f32_e32 v250, 0, v207
	v_sub_f32_e32 v251, 0, v207
.LBB0_1028:
	v_add_u32_e32 v230, s44, v228
	ds_read_b64_tr_b16 v[190:191], v230 offset:49152
	ds_read_b64_tr_b16 v[192:193], v230 offset:49664
	s_waitcnt lgkmcnt(9)
	v_mfma_f32_32x32x16_bf16 v[114:129], v[102:105], v[158:161], v[236:251]
	v_add_f32_e32 v106, v82, v83
	v_add_f32_e32 v106, v84, v106
	v_add_f32_e32 v106, v85, v106
	v_add_f32_e32 v106, v86, v106
	v_add_f32_e32 v106, v87, v106
	v_cvt_pk_bf16_f32 v150, v82, v83
	v_cvt_pk_bf16_f32 v151, v84, v85
	ds_read_b64_tr_b16 v[186:187], v230 offset:53248
	ds_read_b64_tr_b16 v[188:189], v230 offset:53760
	v_add_f32_e32 v82, v88, v106
	s_waitcnt lgkmcnt(10)
	v_mfma_f32_32x32x16_bf16 v[98:113], v[98:101], v[158:161], v[236:251]
	v_add_f32_e32 v82, v89, v82
	v_add_f32_e32 v82, v90, v82
	v_add_f32_e32 v130, v91, v82
	v_cvt_pk_bf16_f32 v152, v86, v87
	v_cvt_pk_bf16_f32 v153, v88, v89
	ds_read_b64_tr_b16 v[82:83], v230 offset:57344
	ds_read_b64_tr_b16 v[84:85], v230 offset:57856
	s_waitcnt lgkmcnt(11)
	v_mfma_f32_32x32x16_bf16 v[114:129], v[182:185], v[154:157], v[114:129]
	v_add_f32_e32 v86, v92, v130
	v_add_f32_e32 v86, v93, v86
	v_add_f32_e32 v86, v94, v86
	v_add_f32_e32 v130, v95, v86
	v_cvt_pk_bf16_f32 v138, v90, v91
	v_cvt_pk_bf16_f32 v139, v92, v93
	ds_read_b64_tr_b16 v[86:87], v230 offset:61440
	ds_read_b64_tr_b16 v[88:89], v230 offset:61952
	s_waitcnt lgkmcnt(12)
	v_mfma_f32_32x32x16_bf16 v[98:113], v[178:181], v[154:157], v[98:113]
	v_add_f32_e32 v90, v96, v130
	v_add_f32_e32 v90, v97, v90
	v_add_f32_e32 v90, v66, v90
	v_add_f32_e32 v130, v67, v90
	v_cvt_pk_bf16_f32 v140, v94, v95
	v_cvt_pk_bf16_f32 v141, v96, v97
	ds_read_b64_tr_b16 v[90:91], v230 offset:50176
	ds_read_b64_tr_b16 v[92:93], v230 offset:50688
	s_waitcnt lgkmcnt(13)
	v_mfma_f32_32x32x16_bf16 v[114:129], v[174:177], v[146:149], v[114:129]
	v_add_f32_e32 v94, v68, v130
	v_add_f32_e32 v94, v69, v94
	v_add_f32_e32 v94, v70, v94
	v_add_f32_e32 v130, v71, v94
	v_cvt_pk_bf16_f32 v134, v66, v67
	v_cvt_pk_bf16_f32 v135, v68, v69
	ds_read_b64_tr_b16 v[94:95], v230 offset:54272
	ds_read_b64_tr_b16 v[96:97], v230 offset:54784
	s_waitcnt lgkmcnt(14)
	v_mfma_f32_32x32x16_bf16 v[98:113], v[170:173], v[146:149], v[98:113]
	v_add_f32_e32 v66, v72, v130
	v_add_f32_e32 v66, v73, v66
	v_add_f32_e32 v66, v74, v66
	v_add_f32_e32 v66, v75, v66
	v_cvt_pk_bf16_f32 v136, v70, v71
	v_cvt_pk_bf16_f32 v137, v72, v73
	ds_read_b64_tr_b16 v[194:195], v230 offset:58368
	ds_read_b64_tr_b16 v[196:197], v230 offset:58880
	s_waitcnt lgkmcnt(14)
	v_mfma_f32_32x32x16_bf16 v[114:129], v[166:169], v[142:145], v[114:129]
	v_add_f32_e32 v66, v76, v66
	v_add_f32_e32 v66, v77, v66
	v_add_f32_e32 v66, v78, v66
	v_add_f32_e32 v66, v79, v66
	v_cvt_pk_bf16_f32 v130, v74, v75
	v_cvt_pk_bf16_f32 v131, v76, v77
	ds_read_b64_tr_b16 v[74:75], v230 offset:62464
	ds_read_b64_tr_b16 v[76:77], v230 offset:62976
	v_mfma_f32_32x32x16_bf16 v[98:113], v[162:165], v[142:145], v[98:113]
	v_add_f32_e32 v66, v80, v66
	v_add_f32_e32 v66, v81, v66
	v_add_f32_e32 v66, 0, v66
	v_cvt_pk_bf16_f32 v132, v78, v79
	v_cvt_pk_bf16_f32 v133, v80, v81
	s_add_i32 s4, s10, s89
	s_mov_b32 s5, m0
	s_mov_b32 m0, s4
	s_nop 0
	global_load_lds_dwordx4 v[220:221], off
	s_mov_b32 m0, s5
	v_add_f32_e32 v234, v234, v66
	s_addk_i32 s4, 0x400
	s_mov_b32 s5, m0
	s_mov_b32 m0, s4
	s_nop 0
	global_load_lds_dwordx4 v[218:219], off
	s_mov_b32 m0, s5
	v_lshl_add_u64 v[66:67], v[224:225], 0, s[0:1]
	s_add_i32 s4, s9, s70
	s_mov_b32 s5, m0
	s_mov_b32 m0, s4
	s_nop 0
	global_load_lds_dwordx4 v[66:67], off
	s_mov_b32 m0, s5
	v_lshl_add_u64 v[66:67], v[224:225], 0, s[64:65]
	s_addk_i32 s4, 0x400
	s_mov_b32 s5, m0
	s_mov_b32 m0, s4
	s_nop 0
	global_load_lds_dwordx4 v[66:67], off
	s_mov_b32 m0, s5
	v_max_f32_e32 v66, v115, v115
	v_max_f32_e32 v67, v114, v114
	v_max_f32_e32 v66, v67, v66
	v_max3_f32 v67, v116, v117, v99
	v_max3_f32 v66, v66, v98, v100
	v_max3_f32 v66, v66, v101, v118
	v_max3_f32 v67, v67, v120, v121
	v_max3_f32 v66, v66, v119, v102
	v_max3_f32 v67, v67, v104, v105
	v_max3_f32 v66, v66, v103, v122
	v_max3_f32 v67, v67, v124, v125
	v_max3_f32 v66, v66, v123, v106
	v_max3_f32 v67, v67, v108, v109
	v_max3_f32 v66, v66, v107, v126
	v_max3_f32 v67, v67, v128, v129
	v_max3_f32 v66, v66, v127, v110
	v_max3_f32 v67, v67, v112, v113
	v_max3_f32 v66, v66, v111, v67
	v_mov_b32_e32 v67, v66
	s_nop 1
	v_permlane32_swap_b32_e32 v66, v67
	v_max_f32_e32 v67, v67, v67
	v_max_f32_e32 v66, v66, v66
	v_max_f32_e32 v66, v66, v67
	v_cmp_lt_f32_e32 vcc, s3, v66
	s_cmp_lg_u64 vcc, 0
	s_cselect_b64 s[4:5], -1, 0
	s_cbranch_vccnz .LBB0_1036
.LBB0_1029:
	s_add_i32 s6, s9, 0
	v_add_u32_e32 v66, s6, v209
	ds_read_b128 v[70:73], v66
	ds_read_b128 v[66:69], v66 offset:8192
	s_waitcnt lgkmcnt(14)
	v_mfma_f32_32x32x16_bf16 v[2:17], v[150:153], v[190:193], v[2:17]
	v_exp_f32_e32 v114, v114
	v_exp_f32_e32 v115, v115
	v_add_u32_e32 v78, s6, v213
	ds_read_b128 v[182:185], v78
	ds_read_b128 v[178:181], v78 offset:8192
	v_mfma_f32_32x32x16_bf16 v[50:65], v[150:153], v[186:189], v[50:65]
	v_exp_f32_e32 v116, v116
	v_exp_f32_e32 v117, v117
	v_add_u32_e32 v78, s6, v231
	ds_read_b128 v[174:177], v78
	ds_read_b128 v[170:173], v78 offset:8192
	s_waitcnt lgkmcnt(14)
	v_mfma_f32_32x32x16_bf16 v[34:49], v[150:153], v[82:85], v[34:49]
	v_exp_f32_e32 v118, v118
	v_exp_f32_e32 v119, v119
	v_add_u32_e32 v78, s6, v235
	ds_read_b128 v[166:169], v78
	ds_read_b128 v[162:165], v78 offset:8192
	v_mfma_f32_32x32x16_bf16 v[18:33], v[150:153], v[86:89], v[18:33]
	v_exp_f32_e32 v120, v120
	v_exp_f32_e32 v121, v121
	ds_read_b64_tr_b16 v[78:79], v230 offset:51200
	ds_read_b64_tr_b16 v[80:81], v230 offset:51712
	s_waitcnt lgkmcnt(14)
	v_mfma_f32_32x32x16_bf16 v[2:17], v[138:141], v[90:93], v[2:17]
	v_exp_f32_e32 v122, v122
	v_exp_f32_e32 v123, v123
	ds_read_b64_tr_b16 v[82:83], v230 offset:55296
	ds_read_b64_tr_b16 v[84:85], v230 offset:55808
	v_mfma_f32_32x32x16_bf16 v[50:65], v[138:141], v[94:97], v[50:65]
	v_exp_f32_e32 v124, v124
	v_exp_f32_e32 v125, v125
	ds_read_b64_tr_b16 v[86:87], v230 offset:59392
	ds_read_b64_tr_b16 v[88:89], v230 offset:59904
	s_waitcnt lgkmcnt(14)
	v_mfma_f32_32x32x16_bf16 v[34:49], v[138:141], v[194:197], v[34:49]
	v_exp_f32_e32 v126, v126
	v_exp_f32_e32 v127, v127
	ds_read_b64_tr_b16 v[90:91], v230 offset:63488
	ds_read_b64_tr_b16 v[92:93], v230 offset:64000
	v_mfma_f32_32x32x16_bf16 v[18:33], v[138:141], v[74:77], v[18:33]
	v_exp_f32_e32 v128, v128
	v_exp_f32_e32 v129, v129
	ds_read_b64_tr_b16 v[74:75], v230 offset:52224
	ds_read_b64_tr_b16 v[76:77], v230 offset:52736
	s_waitcnt lgkmcnt(8)
	v_mfma_f32_32x32x16_bf16 v[2:17], v[134:137], v[78:81], v[2:17]
	v_exp_f32_e32 v98, v98
	v_exp_f32_e32 v99, v99
	ds_read_b64_tr_b16 v[78:79], v230 offset:56320
	ds_read_b64_tr_b16 v[80:81], v230 offset:56832
	s_waitcnt lgkmcnt(8)
	v_mfma_f32_32x32x16_bf16 v[50:65], v[134:137], v[82:85], v[50:65]
	v_exp_f32_e32 v100, v100
	v_exp_f32_e32 v101, v101
	ds_read_b64_tr_b16 v[82:83], v230 offset:60416
	ds_read_b64_tr_b16 v[84:85], v230 offset:60928
	s_waitcnt lgkmcnt(8)
	v_mfma_f32_32x32x16_bf16 v[34:49], v[134:137], v[86:89], v[34:49]
	v_exp_f32_e32 v102, v102
	v_exp_f32_e32 v103, v103
	ds_read_b64_tr_b16 v[86:87], v230 offset:64512
	ds_read_b64_tr_b16 v[88:89], v230 offset:65024
	s_waitcnt lgkmcnt(8)
	v_mfma_f32_32x32x16_bf16 v[18:33], v[134:137], v[90:93], v[18:33]
	v_exp_f32_e32 v104, v104
	v_exp_f32_e32 v105, v105
	s_waitcnt lgkmcnt(6)
	v_mfma_f32_32x32x16_bf16 v[2:17], v[130:133], v[74:77], v[2:17]
	v_exp_f32_e32 v106, v106
	v_exp_f32_e32 v107, v107
	s_waitcnt lgkmcnt(4)
	v_mfma_f32_32x32x16_bf16 v[50:65], v[130:133], v[78:81], v[50:65]
	v_exp_f32_e32 v108, v108
	v_exp_f32_e32 v109, v109
	s_waitcnt lgkmcnt(2)
	v_mfma_f32_32x32x16_bf16 v[34:49], v[130:133], v[82:85], v[34:49]
	v_exp_f32_e32 v110, v110
	v_exp_f32_e32 v111, v111
	s_waitcnt lgkmcnt(0)
	v_mfma_f32_32x32x16_bf16 v[18:33], v[130:133], v[86:89], v[18:33]
	v_exp_f32_e32 v112, v112
	v_exp_f32_e32 v113, v113
	s_waitcnt vmcnt(4) lgkmcnt(0)
	s_barrier
	s_andn2_b64 vcc, exec, s[4:5]
	s_cbranch_vccnz .LBB0_1031
	v_add_u32_e32 v86, s20, v229
	ds_read_b128 v[74:77], v86 offset:96
	ds_read_b128 v[78:81], v86 offset:64
	ds_read_b128 v[82:85], v86 offset:32
	ds_read_b128 v[86:89], v86
	s_waitcnt lgkmcnt(3)
	v_pk_mul_f32 v[14:15], v[14:15], v[74:75]
	s_waitcnt lgkmcnt(2)
	v_pk_mul_f32 v[10:11], v[10:11], v[78:79]
	s_waitcnt lgkmcnt(1)
	v_pk_mul_f32 v[6:7], v[6:7], v[82:83]
	v_pk_mul_f32 v[16:17], v[16:17], v[76:77]
	v_pk_mul_f32 v[12:13], v[12:13], v[80:81]
	v_pk_mul_f32 v[8:9], v[8:9], v[84:85]
	s_waitcnt lgkmcnt(0)
	v_pk_mul_f32 v[4:5], v[4:5], v[88:89]
	v_pk_mul_f32 v[2:3], v[2:3], v[86:87]
	v_pk_mul_f32 v[62:63], v[62:63], v[74:75]
	v_pk_mul_f32 v[58:59], v[58:59], v[78:79]
	v_pk_mul_f32 v[54:55], v[54:55], v[82:83]
	v_pk_mul_f32 v[64:65], v[64:65], v[76:77]
	v_pk_mul_f32 v[60:61], v[60:61], v[80:81]
	v_pk_mul_f32 v[56:57], v[56:57], v[84:85]
	v_pk_mul_f32 v[52:53], v[52:53], v[88:89]
	v_pk_mul_f32 v[50:51], v[50:51], v[86:87]
	v_pk_mul_f32 v[46:47], v[46:47], v[74:75]
	v_pk_mul_f32 v[42:43], v[42:43], v[78:79]
	v_pk_mul_f32 v[38:39], v[38:39], v[82:83]
	v_pk_mul_f32 v[48:49], v[48:49], v[76:77]
	v_pk_mul_f32 v[44:45], v[44:45], v[80:81]
	v_pk_mul_f32 v[40:41], v[40:41], v[84:85]
	v_pk_mul_f32 v[36:37], v[36:37], v[88:89]
	v_pk_mul_f32 v[34:35], v[34:35], v[86:87]
	v_pk_mul_f32 v[30:31], v[30:31], v[74:75]
	v_pk_mul_f32 v[26:27], v[26:27], v[78:79]
	v_pk_mul_f32 v[22:23], v[22:23], v[82:83]
	v_pk_mul_f32 v[32:33], v[32:33], v[76:77]
	v_pk_mul_f32 v[28:29], v[28:29], v[80:81]
	v_pk_mul_f32 v[24:25], v[24:25], v[84:85]
	v_pk_mul_f32 v[20:21], v[20:21], v[88:89]
	v_pk_mul_f32 v[18:19], v[18:19], v[86:87]
.LBB0_1031:
	s_add_i32 s4, s9, 0x4000
	s_cmpk_lg_u32 s9, 0x8000
	s_cselect_b32 s11, s4, 0
	v_add_u32_e32 v230, s10, v228
	ds_read_b64_tr_b16 v[190:191], v230 offset:49152
	ds_read_b64_tr_b16 v[192:193], v230 offset:49664
	v_mfma_f32_32x32x16_bf16 v[82:97], v[70:73], v[158:161], v[236:251]
	v_add_f32_e32 v74, v114, v115
	v_add_f32_e32 v74, v116, v74
	v_add_f32_e32 v74, v117, v74
	v_add_f32_e32 v74, v118, v74
	v_add_f32_e32 v74, v119, v74
	v_cvt_pk_bf16_f32 v150, v114, v115
	v_cvt_pk_bf16_f32 v151, v116, v117
	ds_read_b64_tr_b16 v[186:187], v230 offset:53248
	ds_read_b64_tr_b16 v[188:189], v230 offset:53760
	v_add_f32_e32 v70, v120, v74
	v_add_f32_e32 v70, v121, v70
	v_add_f32_e32 v70, v122, v70
	v_add_f32_e32 v130, v123, v70
	v_mfma_f32_32x32x16_bf16 v[66:81], v[66:69], v[158:161], v[236:251]
	v_cvt_pk_bf16_f32 v152, v118, v119
	v_cvt_pk_bf16_f32 v153, v120, v121
	ds_read_b64_tr_b16 v[114:115], v230 offset:57344
	ds_read_b64_tr_b16 v[116:117], v230 offset:57856
	v_mfma_f32_32x32x16_bf16 v[82:97], v[182:185], v[154:157], v[82:97]
	v_add_f32_e32 v118, v124, v130
	v_add_f32_e32 v118, v125, v118
	v_add_f32_e32 v118, v126, v118
	v_add_f32_e32 v130, v127, v118
	v_cvt_pk_bf16_f32 v138, v122, v123
	v_cvt_pk_bf16_f32 v139, v124, v125
	ds_read_b64_tr_b16 v[118:119], v230 offset:61440
	ds_read_b64_tr_b16 v[120:121], v230 offset:61952
	v_mfma_f32_32x32x16_bf16 v[66:81], v[178:181], v[154:157], v[66:81]
	v_add_f32_e32 v122, v128, v130
	v_add_f32_e32 v122, v129, v122
	v_add_f32_e32 v122, v98, v122
	v_add_f32_e32 v130, v99, v122
	v_cvt_pk_bf16_f32 v140, v126, v127
	v_cvt_pk_bf16_f32 v141, v128, v129
	ds_read_b64_tr_b16 v[122:123], v230 offset:50176
	ds_read_b64_tr_b16 v[124:125], v230 offset:50688
	v_mfma_f32_32x32x16_bf16 v[82:97], v[174:177], v[146:149], v[82:97]
	v_add_f32_e32 v126, v100, v130
	v_add_f32_e32 v126, v101, v126
	v_add_f32_e32 v126, v102, v126
	v_add_f32_e32 v130, v103, v126
	v_cvt_pk_bf16_f32 v134, v98, v99
	v_cvt_pk_bf16_f32 v135, v100, v101
	ds_read_b64_tr_b16 v[126:127], v230 offset:54272
	ds_read_b64_tr_b16 v[128:129], v230 offset:54784
	v_mfma_f32_32x32x16_bf16 v[66:81], v[170:173], v[146:149], v[66:81]
	v_add_f32_e32 v98, v104, v130
	v_add_f32_e32 v98, v105, v98
	v_add_f32_e32 v98, v106, v98
	v_add_f32_e32 v98, v107, v98
	v_cvt_pk_bf16_f32 v136, v102, v103
	v_cvt_pk_bf16_f32 v137, v104, v105
	ds_read_b64_tr_b16 v[194:195], v230 offset:58368
	ds_read_b64_tr_b16 v[196:197], v230 offset:58880
	v_mfma_f32_32x32x16_bf16 v[82:97], v[166:169], v[142:145], v[82:97]
	v_add_f32_e32 v98, v108, v98
	v_add_f32_e32 v98, v109, v98
	v_add_f32_e32 v98, v110, v98
	v_add_f32_e32 v98, v111, v98
	v_cvt_pk_bf16_f32 v130, v106, v107
	v_cvt_pk_bf16_f32 v131, v108, v109
	ds_read_b64_tr_b16 v[106:107], v230 offset:62464
	ds_read_b64_tr_b16 v[108:109], v230 offset:62976
	v_mfma_f32_32x32x16_bf16 v[66:81], v[162:165], v[142:145], v[66:81]
	v_add_f32_e32 v98, v112, v98
	v_add_f32_e32 v98, v113, v98
	v_add_f32_e32 v98, 0, v98
	v_cvt_pk_bf16_f32 v132, v110, v111
	v_cvt_pk_bf16_f32 v133, v112, v113
	s_nop 0
	v_add_f32_e32 v234, v234, v98
	s_add_i32 s4, s9, s89
	v_lshl_add_u64 v[98:99], v[220:221], 0, s[0:1]
	s_mov_b32 s5, m0
	s_mov_b32 m0, s4
	s_nop 0
	global_load_lds_dwordx4 v[98:99], off
	s_mov_b32 m0, s5
	v_lshl_add_u64 v[98:99], v[218:219], 0, s[0:1]
	s_addk_i32 s4, 0x400
	s_mov_b32 s5, m0
	s_mov_b32 m0, s4
	s_nop 0
	global_load_lds_dwordx4 v[98:99], off
	s_mov_b32 m0, s5
	v_lshl_add_u64 v[110:111], v[224:225], 0, s[74:75]
	s_add_i32 s4, s11, s70
	s_mov_b32 s5, m0
	s_mov_b32 m0, s4
	s_nop 0
	global_load_lds_dwordx4 v[110:111], off
	s_mov_b32 m0, s5
	v_lshl_add_u64 v[98:99], v[224:225], 0, s[62:63]
	s_addk_i32 s4, 0x400
	s_mov_b32 s5, m0
	s_mov_b32 m0, s4
	s_nop 0
	global_load_lds_dwordx4 v[98:99], off
	s_mov_b32 m0, s5
	v_max_f32_e32 v98, v83, v83
	v_max_f32_e32 v99, v82, v82
	v_max_f32_e32 v98, v99, v98
	v_max3_f32 v99, v84, v85, v67
	v_max3_f32 v98, v98, v66, v68
	v_max3_f32 v98, v98, v69, v86
	v_max3_f32 v99, v99, v88, v89
	v_max3_f32 v98, v98, v87, v70
	v_max3_f32 v99, v99, v72, v73
	v_max3_f32 v98, v98, v71, v90
	v_max3_f32 v99, v99, v92, v93
	v_max3_f32 v98, v98, v91, v74
	v_max3_f32 v99, v99, v76, v77
	v_max3_f32 v98, v98, v75, v94
	v_max3_f32 v99, v99, v96, v97
	v_max3_f32 v98, v98, v95, v78
	v_max3_f32 v99, v99, v80, v81
	v_max3_f32 v98, v98, v79, v99
	v_mov_b32_e32 v99, v98
	s_nop 1
	v_permlane32_swap_b32_e32 v98, v99
	v_max_f32_e32 v99, v99, v99
	v_max_f32_e32 v98, v98, v98
	v_max_f32_e32 v98, v98, v99
	v_cmp_lt_f32_e32 vcc, s3, v98
	s_cmp_lg_u64 vcc, 0
	s_cselect_b64 s[4:5], -1, 0
	s_cbranch_vccnz .LBB0_1039
.LBB0_1032:
	s_add_i32 s6, s11, 0
	v_add_u32_e32 v98, s6, v209
	ds_read_b128 v[102:105], v98
	ds_read_b128 v[98:101], v98 offset:8192
	s_waitcnt lgkmcnt(14)
	v_mfma_f32_32x32x16_bf16 v[2:17], v[150:153], v[190:193], v[2:17]
	v_exp_f32_e32 v82, v82
	v_exp_f32_e32 v83, v83
	v_add_u32_e32 v112, s6, v213
	ds_read_b128 v[182:185], v112
	ds_read_b128 v[178:181], v112 offset:8192
	v_mfma_f32_32x32x16_bf16 v[50:65], v[150:153], v[186:189], v[50:65]
	v_exp_f32_e32 v84, v84
	v_exp_f32_e32 v85, v85
	v_add_u32_e32 v112, s6, v231
	ds_read_b128 v[174:177], v112
	ds_read_b128 v[170:173], v112 offset:8192
	s_waitcnt lgkmcnt(14)
	v_mfma_f32_32x32x16_bf16 v[34:49], v[150:153], v[114:117], v[34:49]
	v_exp_f32_e32 v86, v86
	v_exp_f32_e32 v87, v87
	v_add_u32_e32 v112, s6, v235
	ds_read_b128 v[166:169], v112
	ds_read_b128 v[162:165], v112 offset:8192
	v_mfma_f32_32x32x16_bf16 v[18:33], v[150:153], v[118:121], v[18:33]
	v_exp_f32_e32 v88, v88
	v_exp_f32_e32 v89, v89
	ds_read_b64_tr_b16 v[112:113], v230 offset:51200
	ds_read_b64_tr_b16 v[114:115], v230 offset:51712
	s_waitcnt lgkmcnt(14)
	v_mfma_f32_32x32x16_bf16 v[2:17], v[138:141], v[122:125], v[2:17]
	v_exp_f32_e32 v90, v90
	v_exp_f32_e32 v91, v91
	ds_read_b64_tr_b16 v[116:117], v230 offset:55296
	ds_read_b64_tr_b16 v[118:119], v230 offset:55808
	v_mfma_f32_32x32x16_bf16 v[50:65], v[138:141], v[126:129], v[50:65]
	v_exp_f32_e32 v92, v92
	v_exp_f32_e32 v93, v93
	ds_read_b64_tr_b16 v[120:121], v230 offset:59392
	ds_read_b64_tr_b16 v[122:123], v230 offset:59904
	s_waitcnt lgkmcnt(14)
	v_mfma_f32_32x32x16_bf16 v[34:49], v[138:141], v[194:197], v[34:49]
	v_exp_f32_e32 v94, v94
	v_exp_f32_e32 v95, v95
	ds_read_b64_tr_b16 v[124:125], v230 offset:63488
	ds_read_b64_tr_b16 v[126:127], v230 offset:64000
	v_mfma_f32_32x32x16_bf16 v[18:33], v[138:141], v[106:109], v[18:33]
	v_exp_f32_e32 v96, v96
	v_exp_f32_e32 v97, v97
	ds_read_b64_tr_b16 v[106:107], v230 offset:52224
	ds_read_b64_tr_b16 v[108:109], v230 offset:52736
	s_waitcnt lgkmcnt(8)
	v_mfma_f32_32x32x16_bf16 v[2:17], v[134:137], v[112:115], v[2:17]
	v_exp_f32_e32 v66, v66
	v_exp_f32_e32 v67, v67
	ds_read_b64_tr_b16 v[112:113], v230 offset:56320
	ds_read_b64_tr_b16 v[114:115], v230 offset:56832
	s_waitcnt lgkmcnt(8)
	v_mfma_f32_32x32x16_bf16 v[50:65], v[134:137], v[116:119], v[50:65]
	v_exp_f32_e32 v68, v68
	v_exp_f32_e32 v69, v69
	ds_read_b64_tr_b16 v[116:117], v230 offset:60416
	ds_read_b64_tr_b16 v[118:119], v230 offset:60928
	s_waitcnt lgkmcnt(8)
	v_mfma_f32_32x32x16_bf16 v[34:49], v[134:137], v[120:123], v[34:49]
	v_exp_f32_e32 v70, v70
	v_exp_f32_e32 v71, v71
	ds_read_b64_tr_b16 v[120:121], v230 offset:64512
	ds_read_b64_tr_b16 v[122:123], v230 offset:65024
	s_waitcnt lgkmcnt(8)
	v_mfma_f32_32x32x16_bf16 v[18:33], v[134:137], v[124:127], v[18:33]
	v_exp_f32_e32 v72, v72
	v_exp_f32_e32 v73, v73
	s_waitcnt lgkmcnt(6)
	v_mfma_f32_32x32x16_bf16 v[2:17], v[130:133], v[106:109], v[2:17]
	v_exp_f32_e32 v74, v74
	v_exp_f32_e32 v75, v75
	s_waitcnt lgkmcnt(4)
	v_mfma_f32_32x32x16_bf16 v[50:65], v[130:133], v[112:115], v[50:65]
	v_exp_f32_e32 v76, v76
	v_exp_f32_e32 v77, v77
	s_waitcnt lgkmcnt(2)
	v_mfma_f32_32x32x16_bf16 v[34:49], v[130:133], v[116:119], v[34:49]
	v_exp_f32_e32 v78, v78
	v_exp_f32_e32 v79, v79
	s_waitcnt lgkmcnt(0)
	v_mfma_f32_32x32x16_bf16 v[18:33], v[130:133], v[120:123], v[18:33]
	v_exp_f32_e32 v80, v80
	v_exp_f32_e32 v81, v81
	s_waitcnt vmcnt(4) lgkmcnt(0)
	s_barrier
	s_andn2_b64 vcc, exec, s[4:5]
	s_cbranch_vccnz .LBB0_1034
	v_add_u32_e32 v120, s20, v229
	ds_read_b128 v[106:109], v120 offset:96
	ds_read_b128 v[112:115], v120 offset:64
	ds_read_b128 v[116:119], v120 offset:32
	ds_read_b128 v[120:123], v120
	s_waitcnt lgkmcnt(3)
	v_pk_mul_f32 v[14:15], v[14:15], v[106:107]
	s_waitcnt lgkmcnt(2)
	v_pk_mul_f32 v[10:11], v[10:11], v[112:113]
	s_waitcnt lgkmcnt(1)
	v_pk_mul_f32 v[6:7], v[6:7], v[116:117]
	v_pk_mul_f32 v[16:17], v[16:17], v[108:109]
	v_pk_mul_f32 v[12:13], v[12:13], v[114:115]
	v_pk_mul_f32 v[8:9], v[8:9], v[118:119]
	s_waitcnt lgkmcnt(0)
	v_pk_mul_f32 v[4:5], v[4:5], v[122:123]
	v_pk_mul_f32 v[2:3], v[2:3], v[120:121]
	v_pk_mul_f32 v[62:63], v[62:63], v[106:107]
	v_pk_mul_f32 v[58:59], v[58:59], v[112:113]
	v_pk_mul_f32 v[54:55], v[54:55], v[116:117]
	v_pk_mul_f32 v[64:65], v[64:65], v[108:109]
	v_pk_mul_f32 v[60:61], v[60:61], v[114:115]
	v_pk_mul_f32 v[56:57], v[56:57], v[118:119]
	v_pk_mul_f32 v[52:53], v[52:53], v[122:123]
	v_pk_mul_f32 v[50:51], v[50:51], v[120:121]
	v_pk_mul_f32 v[46:47], v[46:47], v[106:107]
	v_pk_mul_f32 v[42:43], v[42:43], v[112:113]
	v_pk_mul_f32 v[38:39], v[38:39], v[116:117]
	v_pk_mul_f32 v[48:49], v[48:49], v[108:109]
	v_pk_mul_f32 v[44:45], v[44:45], v[114:115]
	v_pk_mul_f32 v[40:41], v[40:41], v[118:119]
	v_pk_mul_f32 v[36:37], v[36:37], v[122:123]
	v_pk_mul_f32 v[34:35], v[34:35], v[120:121]
	v_pk_mul_f32 v[30:31], v[30:31], v[106:107]
	v_pk_mul_f32 v[26:27], v[26:27], v[112:113]
	v_pk_mul_f32 v[22:23], v[22:23], v[116:117]
	v_pk_mul_f32 v[32:33], v[32:33], v[108:109]
	v_pk_mul_f32 v[28:29], v[28:29], v[114:115]
	v_pk_mul_f32 v[24:25], v[24:25], v[118:119]
	v_pk_mul_f32 v[20:21], v[20:21], v[122:123]
	v_pk_mul_f32 v[18:19], v[18:19], v[120:121]

.LBB0_1036:
	v_max_f32_e32 v66, v66, v66
	v_max_f32_e32 v67, 0, v66
	v_exp_f32_e64 v66, -v67
	s_and_saveexec_b64 s[6:7], s[40:41]
	ds_write_b32 v205, v66
	s_or_b64 exec, exec, s[6:7]
	v_sub_f32_e32 v98, v98, v67
	v_sub_f32_e32 v99, v99, v67
	v_sub_f32_e32 v100, v100, v67
	v_sub_f32_e32 v101, v101, v67
	v_sub_f32_e32 v102, v102, v67
	v_sub_f32_e32 v103, v103, v67
	v_sub_f32_e32 v104, v104, v67
	v_sub_f32_e32 v105, v105, v67
	v_sub_f32_e32 v106, v106, v67
	v_sub_f32_e32 v107, v107, v67
	v_sub_f32_e32 v108, v108, v67
	v_sub_f32_e32 v109, v109, v67
	v_sub_f32_e32 v110, v110, v67
	v_sub_f32_e32 v111, v111, v67
	v_sub_f32_e32 v112, v112, v67
	v_sub_f32_e32 v113, v113, v67
	v_sub_f32_e32 v114, v114, v67
	v_sub_f32_e32 v115, v115, v67
	v_sub_f32_e32 v116, v116, v67
	v_sub_f32_e32 v117, v117, v67
	v_sub_f32_e32 v118, v118, v67
	v_sub_f32_e32 v119, v119, v67
	v_sub_f32_e32 v120, v120, v67
	v_sub_f32_e32 v121, v121, v67
	v_sub_f32_e32 v122, v122, v67
	v_sub_f32_e32 v123, v123, v67
	v_sub_f32_e32 v124, v124, v67
	v_sub_f32_e32 v125, v125, v67
	v_sub_f32_e32 v126, v126, v67
	v_sub_f32_e32 v127, v127, v67
	v_sub_f32_e32 v128, v128, v67
	v_sub_f32_e32 v129, v129, v67
	v_add_f32_e32 v207, v207, v67
	v_sub_f32_e32 v236, 0, v207
	v_sub_f32_e32 v237, 0, v207
	v_sub_f32_e32 v238, 0, v207
	v_sub_f32_e32 v239, 0, v207
	v_sub_f32_e32 v240, 0, v207
	v_sub_f32_e32 v241, 0, v207
	v_sub_f32_e32 v242, 0, v207
	v_sub_f32_e32 v243, 0, v207
	v_sub_f32_e32 v244, 0, v207
	v_sub_f32_e32 v245, 0, v207
	v_sub_f32_e32 v246, 0, v207
	v_sub_f32_e32 v247, 0, v207
	v_sub_f32_e32 v248, 0, v207
	v_sub_f32_e32 v249, 0, v207
	v_sub_f32_e32 v250, 0, v207
	v_sub_f32_e32 v251, 0, v207
	v_mul_f32_e32 v234, v234, v66
	s_branch .LBB0_1029
.LBB0_1039:
	v_max_f32_e32 v98, v98, v98
	v_max_f32_e32 v99, 0, v98
	v_exp_f32_e64 v98, -v99
	s_and_saveexec_b64 s[6:7], s[40:41]
	ds_write_b32 v205, v98
	s_or_b64 exec, exec, s[6:7]
	v_sub_f32_e32 v66, v66, v99
	v_sub_f32_e32 v67, v67, v99
	v_sub_f32_e32 v68, v68, v99
	v_sub_f32_e32 v69, v69, v99
	v_sub_f32_e32 v70, v70, v99
	v_sub_f32_e32 v71, v71, v99
	v_sub_f32_e32 v72, v72, v99
	v_sub_f32_e32 v73, v73, v99
	v_sub_f32_e32 v74, v74, v99
	v_sub_f32_e32 v75, v75, v99
	v_sub_f32_e32 v76, v76, v99
	v_sub_f32_e32 v77, v77, v99
	v_sub_f32_e32 v78, v78, v99
	v_sub_f32_e32 v79, v79, v99
	v_sub_f32_e32 v80, v80, v99
	v_sub_f32_e32 v81, v81, v99
	v_sub_f32_e32 v82, v82, v99
	v_sub_f32_e32 v83, v83, v99
	v_sub_f32_e32 v84, v84, v99
	v_sub_f32_e32 v85, v85, v99
	v_sub_f32_e32 v86, v86, v99
	v_sub_f32_e32 v87, v87, v99
	v_sub_f32_e32 v88, v88, v99
	v_sub_f32_e32 v89, v89, v99
	v_sub_f32_e32 v90, v90, v99
	v_sub_f32_e32 v91, v91, v99
	v_sub_f32_e32 v92, v92, v99
	v_sub_f32_e32 v93, v93, v99
	v_sub_f32_e32 v94, v94, v99
	v_sub_f32_e32 v95, v95, v99
	v_sub_f32_e32 v96, v96, v99
	v_sub_f32_e32 v97, v97, v99
	v_add_f32_e32 v207, v207, v99
	v_sub_f32_e32 v236, 0, v207
	v_sub_f32_e32 v237, 0, v207
	v_sub_f32_e32 v238, 0, v207
	v_sub_f32_e32 v239, 0, v207
	v_sub_f32_e32 v240, 0, v207
	v_sub_f32_e32 v241, 0, v207
	v_sub_f32_e32 v242, 0, v207
	v_sub_f32_e32 v243, 0, v207
	v_sub_f32_e32 v244, 0, v207
	v_sub_f32_e32 v245, 0, v207
	v_sub_f32_e32 v246, 0, v207
	v_sub_f32_e32 v247, 0, v207
	v_sub_f32_e32 v248, 0, v207
	v_sub_f32_e32 v249, 0, v207
	v_sub_f32_e32 v250, 0, v207
	v_sub_f32_e32 v251, 0, v207
	v_mul_f32_e32 v234, v234, v98
	s_branch .LBB0_1032
.LBB0_1042:
	v_mov_b32_e32 v243, v228
	v_mov_b32_e32 v245, v229
	v_mov_b32_e32 v251, v231
	v_mbcnt_lo_u32_b32 v221, -1, 0
	v_mbcnt_hi_u32_b32 v221, -1, v221
	v_and_b32_e32 v221, 32, v221
	v_lshl_add_u32 v221, v221, 2, v205
	ds_read_b32 v237, v221 offset:2048
	ds_read_b32 v238, v221 offset:4096
	ds_read_b32 v239, v221 offset:6144
	ds_read_b32 v240, v221 offset:8192
	ds_read_b32 v241, v221 offset:10240
	ds_read_b32 v242, v221 offset:12288
	ds_read_b32 v244, v221 offset:14336
	ds_read_b32 v246, v221 offset:16384
	s_waitcnt lgkmcnt(0)
	ds_read_b32 v247, v221 offset:18432
	ds_read_b32 v248, v221 offset:20480
	ds_read_b32 v249, v221 offset:22528
	ds_read_b32 v250, v221 offset:24576
	ds_read_b32 v228, v221 offset:26624
	ds_read_b32 v229, v221 offset:28672
	ds_read_b32 v231, v221 offset:30720
	s_waitcnt lgkmcnt(0)
	v_lshl_add_u64 v[216:217], v[216:217], 0, s[76:77]
	v_lshl_add_u64 v[214:215], v[214:215], 0, s[76:77]
	v_lshl_add_u64 v[218:219], v[202:203], 0, v[222:223]
	s_mov_b32 s44, 59
	s_mov_b32 s45, 0
	s_mov_b32 s46, 0x8000
	s_movk_i32 s4, 0x4000
